# index top-k: next row's 64 score loads prefetched into v159-v207/v240-v254 while the current row is bisected (row round trip hidden; the per-load vmcnt ladder replaced by register copies) - stacked on
# speedup vs baseline: 1.0039x; 1.0039x over previous
.LBB0_405:
	s_andn2_b64 vcc, exec, s[0:1]
	s_cbranch_vccnz .LBB0_449
	s_mov_b32 s100, 0
	s_add_i32 s4, s80, 0xffffff70
	s_lshr_b32 s5, s4, 2
	v_mov_b32_e32 v45, v0
	s_and_b32 s6, s80, 3
	s_xor_b32 s12, s5, 63
	s_lshl_b32 s0, s6, 12
	s_lshl_b32 s1, s12, 6
	v_lshlrev_b32_e32 v1, 4, v45
	s_add_i32 s7, s1, s0
	v_and_b32_e32 v36, 0x3f0, v1
	v_ashrrev_i32_e32 v1, 6, v45
	v_add_u32_e32 v2, s7, v1
	v_readlane_b32 s8, v239, 24
	v_mul_lo_u32 v2, v2, s90
	v_readlane_b32 s9, v239, 25
	v_mov_b32_e32 v37, v3
	s_mov_b32 s1, 0x12a03000
	v_lshl_add_u64 v[4:5], v[2:3], 1, s[8:9]
	v_add_u32_e32 v2, 0x200, v45
	v_ashrrev_i32_e32 v38, 6, v2
	v_add_u32_e32 v2, s7, v38
	v_mul_lo_u32 v2, v2, s90
	v_lshl_add_u64 v[6:7], v[2:3], 1, s[8:9]
	v_add_u32_e32 v2, 0x400, v45
	v_ashrrev_i32_e32 v39, 6, v2
	v_add_u32_e32 v2, s7, v39
	v_mul_lo_u32 v2, v2, s90
	v_lshl_add_u64 v[12:13], v[2:3], 1, s[8:9]
	v_add_u32_e32 v2, 0x600, v45
	v_ashrrev_i32_e32 v40, 6, v2
	v_add_u32_e32 v2, s7, v40
	v_mul_lo_u32 v2, v2, s90
	v_lshl_add_u64 v[14:15], v[2:3], 1, s[8:9]
	v_add_u32_e32 v2, 0x800, v45
	v_ashrrev_i32_e32 v41, 6, v2
	v_lshl_add_u64 v[4:5], v[4:5], 0, v[36:37]
	v_add_u32_e32 v2, s7, v41
	v_add_co_u32_e32 v4, vcc, s1, v4
	v_mul_lo_u32 v2, v2, s90
	s_nop 0
	v_addc_co_u32_e32 v5, vcc, 0, v5, vcc
	v_lshl_add_u64 v[6:7], v[6:7], 0, v[36:37]
	v_lshl_add_u64 v[20:21], v[2:3], 1, s[8:9]
	v_add_u32_e32 v2, 0xa00, v45
	v_add_co_u32_e32 v8, vcc, s1, v6
	v_ashrrev_i32_e32 v42, 6, v2
	s_nop 0
	v_addc_co_u32_e32 v9, vcc, 0, v7, vcc
	v_lshl_add_u64 v[12:13], v[12:13], 0, v[36:37]
	v_add_u32_e32 v2, s7, v42
	v_add_co_u32_e32 v12, vcc, s1, v12
	v_mul_lo_u32 v2, v2, s90
	s_nop 0
	v_addc_co_u32_e32 v13, vcc, 0, v13, vcc
	v_lshl_add_u64 v[14:15], v[14:15], 0, v[36:37]
	v_lshl_add_u64 v[22:23], v[2:3], 1, s[8:9]
	v_add_u32_e32 v2, 0xc00, v45
	v_add_co_u32_e32 v16, vcc, s1, v14
	v_ashrrev_i32_e32 v43, 6, v2
	s_nop 0
	v_addc_co_u32_e32 v17, vcc, 0, v15, vcc
	v_lshl_add_u64 v[20:21], v[20:21], 0, v[36:37]
	v_add_u32_e32 v2, s7, v43
	v_add_co_u32_e32 v20, vcc, s1, v20
	v_mul_lo_u32 v2, v2, s90
	global_load_dwordx4 v[4:7], v[4:5], off
	s_nop 0
	global_load_dwordx4 v[8:11], v[8:9], off
	v_addc_co_u32_e32 v21, vcc, 0, v21, vcc
	v_lshl_add_u64 v[22:23], v[22:23], 0, v[36:37]
	v_lshl_add_u64 v[28:29], v[2:3], 1, s[8:9]
	v_add_u32_e32 v2, 0xe00, v45
	v_add_co_u32_e32 v24, vcc, s1, v22
	v_ashrrev_i32_e32 v46, 6, v2
	global_load_dwordx4 v[12:15], v[12:13], off
	s_nop 0
	global_load_dwordx4 v[16:19], v[16:17], off
	v_addc_co_u32_e32 v25, vcc, 0, v23, vcc
	v_lshl_add_u64 v[28:29], v[28:29], 0, v[36:37]
	v_add_u32_e32 v2, s7, v46
	v_add_co_u32_e32 v28, vcc, s1, v28
	v_mul_lo_u32 v2, v2, s90
	global_load_dwordx4 v[20:23], v[20:21], off
	s_nop 0
	global_load_dwordx4 v[24:27], v[24:25], off
	v_addc_co_u32_e32 v29, vcc, 0, v29, vcc
	v_lshl_add_u64 v[32:33], v[2:3], 1, s[8:9]
	global_load_dwordx4 v[28:31], v[28:29], off
	v_lshl_add_u64 v[32:33], v[32:33], 0, v[36:37]
	v_add_co_u32_e32 v32, vcc, 0x12a03000, v32
	v_readlane_b32 s10, v239, 26
	s_nop 0
	v_addc_co_u32_e32 v33, vcc, 0, v33, vcc
	global_load_dwordx4 v[32:35], v[32:33], off
	v_readfirstlane_b32 s1, v45
	s_sub_i32 s51, 64, s5
	s_mov_b32 s10, s7
	s_ashr_i32 s36, s1, 6
	s_lshl_b32 s37, s51, 6
	v_writelane_b32 v236, s6, 43
	s_mul_i32 s1, s6, 0x2080000
	v_readlane_b32 s6, v237, 26
	v_readlane_b32 s7, v237, 27
	s_add_u32 s1, s6, s1
	s_addc_u32 s6, s7, 0
	s_mul_i32 s7, s51, s12
	s_lshl_b32 s7, s7, 13
	s_and_b32 s7, s7, 0x3ffc000
	s_add_u32 s8, s1, s7
	v_add_u32_e32 v2, 0, v36
	s_addc_u32 s9, s6, 0
	v_mad_u64_u32 v[36:37], s[6:7], v1, s91, v[2:3]
	v_writelane_b32 v236, s12, 44
	v_and_b32_e32 v44, 63, v45
	v_writelane_b32 v236, s8, 45
	v_readlane_b32 s11, v239, 27
	s_waitcnt vmcnt(7)
	ds_write_b128 v36, v[4:7]
	v_mad_u64_u32 v[4:5], s[6:7], v38, s91, v[2:3]
	s_waitcnt vmcnt(6)
	ds_write_b128 v4, v[8:11]
	v_mad_u64_u32 v[4:5], s[6:7], v39, s91, v[2:3]
	v_writelane_b32 v236, s9, 46
	s_waitcnt vmcnt(5)
	ds_write_b128 v4, v[12:15]
	v_mad_u64_u32 v[4:5], s[6:7], v40, s91, v[2:3]
	s_waitcnt vmcnt(4)
	ds_write_b128 v4, v[16:19]
	v_mad_u64_u32 v[4:5], s[6:7], v41, s91, v[2:3]
	s_waitcnt vmcnt(3)
	ds_write_b128 v4, v[20:23]
	v_mad_u64_u32 v[4:5], s[6:7], v42, s91, v[2:3]
	s_waitcnt vmcnt(2)
	ds_write_b128 v4, v[24:27]
	v_mad_u64_u32 v[4:5], s[6:7], v43, s91, v[2:3]
	s_waitcnt vmcnt(1)
	ds_write_b128 v4, v[28:31]
	v_mad_u64_u32 v[4:5], s[6:7], v46, s91, v[2:3]
	s_lshl_b32 s6, s51, 1
	s_cmp_ge_i32 s36, s6
	s_waitcnt vmcnt(0)
	ds_write_b128 v4, v[32:35]
	s_waitcnt lgkmcnt(0)
	s_barrier
	s_cbranch_scc1 .LBB0_411
	v_and_b32_e32 v1, 31, v45
	v_or_b32_e32 v101, s0, v1
	v_lshrrev_b32_e32 v2, 1, v44
	v_readlane_b32 s0, v236, 45
	v_and_b32_e32 v2, 16, v2
	v_readlane_b32 s1, v236, 46
	v_add_u32_e32 v135, 0, v2
	v_or_b32_e32 v168, s10, v1
	v_lshl_add_u64 v[46:47], s[0:1], 0, v[2:3]
	v_and_b32_e32 v2, 32, v44
	v_lshl_add_u64 v[48:49], s[2:3], 0, v[2:3]
	s_mov_b32 s7, s36

.LBB0_414:
	v_readlane_b32 s38, v239, 31
	v_readlane_b32 s39, v239, 32
	s_andn2_b64 vcc, exec, s[38:39]
	v_mov_b64_e32 v[4:5], -1
	s_cbranch_vccnz .LBB0_443
	s_mul_i32 s14, s36, s37
	s_lshl_b64 s[80:81], s[14:15], 2
	v_readlane_b32 s82, v236, 45
	v_readlane_b32 s83, v236, 46
	s_add_u32 s80, s82, s80
	s_addc_u32 s81, s83, s81
	s_cmp_eq_u32 s100, 1
	s_cbranch_scc1 .Ltk_have
	global_load_dword v159, v9, s[80:81]
	global_load_dword v160, v11, s[80:81]
	global_load_dword v161, v9, s[80:81] offset:512
	global_load_dword v162, v9, s[80:81] offset:768
	global_load_dword v163, v13, s[80:81]
	global_load_dword v164, v6, s[80:81]
	global_load_dword v165, v8, s[80:81]
	global_load_dword v166, v9, s[80:81] offset:1024
	global_load_dword v167, v10, s[80:81]
	global_load_dword v168, v12, s[80:81]
	global_load_dword v169, v14, s[80:81]
	global_load_dword v170, v15, s[80:81]
	global_load_dword v171, v16, s[80:81]
	global_load_dword v172, v17, s[80:81]
	global_load_dword v173, v18, s[80:81]
	global_load_dword v174, v19, s[80:81]
	global_load_dword v175, v20, s[80:81]
	global_load_dword v176, v21, s[80:81]
	global_load_dword v177, v22, s[80:81]
	global_load_dword v178, v23, s[80:81]
	global_load_dword v179, v24, s[80:81]
	global_load_dword v180, v25, s[80:81]
	global_load_dword v181, v26, s[80:81]
	global_load_dword v182, v27, s[80:81]
	global_load_dword v183, v28, s[80:81]
	global_load_dword v184, v29, s[80:81]
	global_load_dword v185, v30, s[80:81]
	global_load_dword v186, v31, s[80:81]
	global_load_dword v187, v32, s[80:81]
	global_load_dword v188, v33, s[80:81]
	global_load_dword v189, v34, s[80:81]
	global_load_dword v190, v35, s[80:81]
	global_load_dword v191, v36, s[80:81]
	global_load_dword v192, v37, s[80:81]
	global_load_dword v193, v38, s[80:81]
	global_load_dword v194, v39, s[80:81]
	global_load_dword v195, v40, s[80:81]
	global_load_dword v196, v41, s[80:81]
	global_load_dword v197, v42, s[80:81]
	global_load_dword v198, v43, s[80:81]
	global_load_dword v199, v46, s[80:81]
	global_load_dword v200, v47, s[80:81]
	global_load_dword v201, v48, s[80:81]
	global_load_dword v202, v49, s[80:81]
	global_load_dword v203, v50, s[80:81]
	global_load_dword v204, v51, s[80:81]
	global_load_dword v205, v52, s[80:81]
	global_load_dword v206, v53, s[80:81]
	global_load_dword v207, v54, s[80:81]
	global_load_dword v240, v55, s[80:81]
	global_load_dword v241, v56, s[80:81]
	global_load_dword v242, v57, s[80:81]
	global_load_dword v243, v58, s[80:81]
	global_load_dword v244, v59, s[80:81]
	global_load_dword v245, v60, s[80:81]
	global_load_dword v246, v61, s[80:81]
	global_load_dword v247, v62, s[80:81]
	global_load_dword v248, v63, s[80:81]
	global_load_dword v249, v64, s[80:81]
	global_load_dword v250, v65, s[80:81]
	global_load_dword v251, v66, s[80:81]
	global_load_dword v252, v67, s[80:81]
	global_load_dword v253, v68, s[80:81]
	global_load_dword v254, v69, s[80:81]
	s_waitcnt vmcnt(0)
	s_branch .Ltk_mov
.Ltk_have:
	s_waitcnt vmcnt(1)
.Ltk_mov:
	v_mov_b32_e32 v1, v159
	v_mov_b32_e32 v2, v160
	v_mov_b32_e32 v4, v161
	v_mov_b32_e32 v70, v162
	v_mov_b32_e32 v71, v163
	v_mov_b32_e32 v72, v164
	v_mov_b32_e32 v73, v165
	v_mov_b32_e32 v74, v166
	v_mov_b32_e32 v75, v167
	v_mov_b32_e32 v76, v168
	v_mov_b32_e32 v77, v169
	v_mov_b32_e32 v78, v170
	v_mov_b32_e32 v79, v171
	v_mov_b32_e32 v80, v172
	v_mov_b32_e32 v81, v173
	v_mov_b32_e32 v82, v174
	v_mov_b32_e32 v83, v175
	v_mov_b32_e32 v84, v176
	v_mov_b32_e32 v85, v177
	v_mov_b32_e32 v86, v178
	v_mov_b32_e32 v87, v179
	v_mov_b32_e32 v88, v180
	v_mov_b32_e32 v89, v181
	v_mov_b32_e32 v90, v182
	v_mov_b32_e32 v91, v183
	v_mov_b32_e32 v92, v184
	v_mov_b32_e32 v93, v185
	v_mov_b32_e32 v94, v186
	v_mov_b32_e32 v95, v187
	v_mov_b32_e32 v96, v188
	v_mov_b32_e32 v97, v189
	v_mov_b32_e32 v98, v190
	v_mov_b32_e32 v99, v191
	v_mov_b32_e32 v100, v192
	v_mov_b32_e32 v101, v193
	v_mov_b32_e32 v103, v194
	v_mov_b32_e32 v104, v195
	v_mov_b32_e32 v105, v196
	v_mov_b32_e32 v106, v197
	v_mov_b32_e32 v107, v198
	v_mov_b32_e32 v108, v199
	v_mov_b32_e32 v110, v200
	v_mov_b32_e32 v112, v201
	v_mov_b32_e32 v113, v202
	v_mov_b32_e32 v114, v203
	v_mov_b32_e32 v115, v204
	v_mov_b32_e32 v116, v205
	v_mov_b32_e32 v117, v206
	v_mov_b32_e32 v118, v207
	v_mov_b32_e32 v119, v240
	v_mov_b32_e32 v120, v241
	v_mov_b32_e32 v121, v242
	v_mov_b32_e32 v122, v243
	v_mov_b32_e32 v123, v244
	v_mov_b32_e32 v124, v245
	v_mov_b32_e32 v125, v246
	v_mov_b32_e32 v126, v247
	v_mov_b32_e32 v127, v248
	v_mov_b32_e32 v128, v249
	v_mov_b32_e32 v129, v250
	v_mov_b32_e32 v130, v251
	v_mov_b32_e32 v131, v252
	v_mov_b32_e32 v133, v253
	v_mov_b32_e32 v134, v254
	s_mov_b32 s100, 0
	s_add_i32 s98, s36, 8
	s_cmpk_lt_u32 s98, 0x40
	s_cbranch_scc0 .Ltk_nopf
	s_lshl_b32 s98, s37, 5
	s_add_u32 s80, s80, s98
	s_addc_u32 s81, s81, 0
	global_load_dword v159, v9, s[80:81]
	global_load_dword v160, v11, s[80:81]
	global_load_dword v161, v9, s[80:81] offset:512
	global_load_dword v162, v9, s[80:81] offset:768
	global_load_dword v163, v13, s[80:81]
	global_load_dword v164, v6, s[80:81]
	global_load_dword v165, v8, s[80:81]
	global_load_dword v166, v9, s[80:81] offset:1024
	global_load_dword v167, v10, s[80:81]
	global_load_dword v168, v12, s[80:81]
	global_load_dword v169, v14, s[80:81]
	global_load_dword v170, v15, s[80:81]
	global_load_dword v171, v16, s[80:81]
	global_load_dword v172, v17, s[80:81]
	global_load_dword v173, v18, s[80:81]
	global_load_dword v174, v19, s[80:81]
	global_load_dword v175, v20, s[80:81]
	global_load_dword v176, v21, s[80:81]
	global_load_dword v177, v22, s[80:81]
	global_load_dword v178, v23, s[80:81]
	global_load_dword v179, v24, s[80:81]
	global_load_dword v180, v25, s[80:81]
	global_load_dword v181, v26, s[80:81]
	global_load_dword v182, v27, s[80:81]
	global_load_dword v183, v28, s[80:81]
	global_load_dword v184, v29, s[80:81]
	global_load_dword v185, v30, s[80:81]
	global_load_dword v186, v31, s[80:81]
	global_load_dword v187, v32, s[80:81]
	global_load_dword v188, v33, s[80:81]
	global_load_dword v189, v34, s[80:81]
	global_load_dword v190, v35, s[80:81]
	global_load_dword v191, v36, s[80:81]
	global_load_dword v192, v37, s[80:81]
	global_load_dword v193, v38, s[80:81]
	global_load_dword v194, v39, s[80:81]
	global_load_dword v195, v40, s[80:81]
	global_load_dword v196, v41, s[80:81]
	global_load_dword v197, v42, s[80:81]
	global_load_dword v198, v43, s[80:81]
	global_load_dword v199, v46, s[80:81]
	global_load_dword v200, v47, s[80:81]
	global_load_dword v201, v48, s[80:81]
	global_load_dword v202, v49, s[80:81]
	global_load_dword v203, v50, s[80:81]
	global_load_dword v204, v51, s[80:81]
	global_load_dword v205, v52, s[80:81]
	global_load_dword v206, v53, s[80:81]
	global_load_dword v207, v54, s[80:81]
	global_load_dword v240, v55, s[80:81]
	global_load_dword v241, v56, s[80:81]
	global_load_dword v242, v57, s[80:81]
	global_load_dword v243, v58, s[80:81]
	global_load_dword v244, v59, s[80:81]
	global_load_dword v245, v60, s[80:81]
	global_load_dword v246, v61, s[80:81]
	global_load_dword v247, v62, s[80:81]
	global_load_dword v248, v63, s[80:81]
	global_load_dword v249, v64, s[80:81]
	global_load_dword v250, v65, s[80:81]
	global_load_dword v251, v66, s[80:81]
	global_load_dword v252, v67, s[80:81]
	global_load_dword v253, v68, s[80:81]
	global_load_dword v254, v69, s[80:81]
	s_mov_b32 s100, 1
.Ltk_nopf:
	v_readlane_b32 s80, v236, 47
	v_readlane_b32 s81, v236, 48
	s_mov_b32 s39, s97
	s_mov_b32 s38, s96
	s_mov_b32 s14, 0
	v_not_b32_e32 v5, v1
	v_or_b32_e32 v102, 0x80000000, v1
	v_cmp_gt_i32_e32 vcc, 0, v1
	v_not_b32_e32 v1, v2
	s_nop 0
	v_cndmask_b32_e32 v111, v102, v5, vcc
	v_or_b32_e32 v5, 0x80000000, v2
	v_cmp_gt_i32_e32 vcc, 0, v2
	v_or_b32_e32 v2, 0x80000000, v4
	v_cndmask_b32_e32 v135, v5, v1, vcc
	v_not_b32_e32 v1, v4
	v_cmp_gt_i32_e32 vcc, 0, v4
	v_and_b32_e32 v5, 0x7fffffff, v70
	v_and_b32_e32 v4, 0x7fffffff, v74
	v_cndmask_b32_e32 v109, v2, v1, vcc
	v_xor_b32_e32 v1, -1, v70
	v_pk_add_f32 v[4:5], v[4:5], 0 neg_lo:[1,1] neg_hi:[1,1]
	v_cmp_gt_i32_e32 vcc, 0, v70
	v_xor_b32_e32 v2, -1, v74
	s_nop 0
	v_cndmask_b32_e32 v1, v5, v1, vcc
	v_cmp_gt_i32_e32 vcc, 0, v74
	v_or_b32_e32 v5, 0x80000000, v71
	v_or_b32_e32 v74, 0x80000000, v77
	v_cndmask_b32_e32 v2, v4, v2, vcc
	v_not_b32_e32 v4, v71
	v_cmp_gt_i32_e32 vcc, 0, v71
	s_nop 1
	v_cndmask_b32_e32 v70, v5, v4, vcc
	v_not_b32_e32 v4, v72
	v_or_b32_e32 v5, 0x80000000, v72
	v_cmp_gt_i32_e32 vcc, 0, v72
	s_nop 1
	v_cndmask_b32_e32 v71, v5, v4, vcc
	v_not_b32_e32 v4, v73
	v_or_b32_e32 v5, 0x80000000, v73
	v_cmp_gt_i32_e32 vcc, 0, v73
	v_or_b32_e32 v73, 0x80000000, v76
	s_nop 0
	v_cndmask_b32_e32 v72, v5, v4, vcc
	v_not_b32_e32 v4, v75
	v_or_b32_e32 v5, 0x80000000, v75
	v_cmp_gt_i32_e32 vcc, 0, v75
	v_or_b32_e32 v75, 0x80000000, v78
	v_cndmask_b32_e32 v4, v5, v4, vcc
	v_not_b32_e32 v5, v76
	v_cmp_gt_i32_e32 vcc, 0, v76
	v_or_b32_e32 v76, 0x80000000, v79
	v_cndmask_b32_e32 v73, v73, v5, vcc
	v_not_b32_e32 v5, v77
	v_cmp_gt_i32_e32 vcc, 0, v77
	v_or_b32_e32 v77, 0x80000000, v80
	v_cndmask_b32_e32 v74, v74, v5, vcc
	v_not_b32_e32 v5, v78
	v_cmp_gt_i32_e32 vcc, 0, v78
	v_or_b32_e32 v78, 0x80000000, v81
	v_cndmask_b32_e32 v75, v75, v5, vcc
	v_not_b32_e32 v5, v79
	v_cmp_gt_i32_e32 vcc, 0, v79
	v_or_b32_e32 v79, 0x80000000, v82
	v_cndmask_b32_e32 v76, v76, v5, vcc
	v_not_b32_e32 v5, v80
	v_cmp_gt_i32_e32 vcc, 0, v80
	v_or_b32_e32 v80, 0x80000000, v83
	v_cndmask_b32_e32 v77, v77, v5, vcc
	v_not_b32_e32 v5, v81
	v_cmp_gt_i32_e32 vcc, 0, v81
	v_or_b32_e32 v81, 0x80000000, v84
	v_cndmask_b32_e32 v78, v78, v5, vcc
	v_not_b32_e32 v5, v82
	v_cmp_gt_i32_e32 vcc, 0, v82
	v_or_b32_e32 v82, 0x80000000, v85
	v_cndmask_b32_e32 v79, v79, v5, vcc
	v_not_b32_e32 v5, v83
	v_cmp_gt_i32_e32 vcc, 0, v83
	v_or_b32_e32 v83, 0x80000000, v86
	v_cndmask_b32_e32 v5, v80, v5, vcc
	v_not_b32_e32 v80, v84
	v_cmp_gt_i32_e32 vcc, 0, v84
	v_or_b32_e32 v84, 0x80000000, v87
	v_cndmask_b32_e32 v80, v81, v80, vcc
	v_not_b32_e32 v81, v85
	v_cmp_gt_i32_e32 vcc, 0, v85
	v_or_b32_e32 v85, 0x80000000, v88
	v_cndmask_b32_e32 v81, v82, v81, vcc
	v_not_b32_e32 v82, v86
	v_cmp_gt_i32_e32 vcc, 0, v86
	v_or_b32_e32 v86, 0x80000000, v89
	v_cndmask_b32_e32 v82, v83, v82, vcc
	v_not_b32_e32 v83, v87
	v_cmp_gt_i32_e32 vcc, 0, v87
	v_or_b32_e32 v87, 0x80000000, v90
	v_cndmask_b32_e32 v83, v84, v83, vcc
	v_not_b32_e32 v84, v88
	v_cmp_gt_i32_e32 vcc, 0, v88
	v_or_b32_e32 v88, 0x80000000, v91
	v_cndmask_b32_e32 v84, v85, v84, vcc
	v_not_b32_e32 v85, v89
	v_cmp_gt_i32_e32 vcc, 0, v89
	v_or_b32_e32 v89, 0x80000000, v92
	v_cndmask_b32_e32 v85, v86, v85, vcc
	v_not_b32_e32 v86, v90
	v_cmp_gt_i32_e32 vcc, 0, v90
	v_or_b32_e32 v90, 0x80000000, v93
	v_cndmask_b32_e32 v86, v87, v86, vcc
	v_not_b32_e32 v87, v91
	v_cmp_gt_i32_e32 vcc, 0, v91
	v_or_b32_e32 v91, 0x80000000, v94
	v_cndmask_b32_e32 v87, v88, v87, vcc
	v_not_b32_e32 v88, v92
	v_cmp_gt_i32_e32 vcc, 0, v92
	v_or_b32_e32 v92, 0x80000000, v95
	v_cndmask_b32_e32 v88, v89, v88, vcc
	v_not_b32_e32 v89, v93
	v_cmp_gt_i32_e32 vcc, 0, v93
	v_or_b32_e32 v93, 0x80000000, v96
	v_cndmask_b32_e32 v89, v90, v89, vcc
	v_not_b32_e32 v90, v94
	v_cmp_gt_i32_e32 vcc, 0, v94
	v_or_b32_e32 v94, 0x80000000, v97
	v_cndmask_b32_e32 v90, v91, v90, vcc
	v_not_b32_e32 v91, v95
	v_cmp_gt_i32_e32 vcc, 0, v95
	v_or_b32_e32 v95, 0x80000000, v98
	v_cndmask_b32_e32 v91, v92, v91, vcc
	v_not_b32_e32 v92, v96
	v_cmp_gt_i32_e32 vcc, 0, v96
	v_or_b32_e32 v96, 0x80000000, v99
	v_cndmask_b32_e32 v92, v93, v92, vcc
	v_not_b32_e32 v93, v97
	v_cmp_gt_i32_e32 vcc, 0, v97
	v_or_b32_e32 v97, 0x80000000, v101
	v_cndmask_b32_e32 v93, v94, v93, vcc
	v_not_b32_e32 v94, v98
	v_cmp_gt_i32_e32 vcc, 0, v98
	v_or_b32_e32 v98, 0x80000000, v103
	v_cndmask_b32_e32 v94, v95, v94, vcc
	v_not_b32_e32 v95, v99
	v_cmp_gt_i32_e32 vcc, 0, v99
	v_or_b32_e32 v99, 0x80000000, v104
	v_cndmask_b32_e32 v102, v96, v95, vcc
	v_not_b32_e32 v95, v100
	v_or_b32_e32 v96, 0x80000000, v100
	v_cmp_gt_i32_e32 vcc, 0, v100
	s_nop 1
	v_cndmask_b32_e32 v95, v96, v95, vcc
	v_not_b32_e32 v96, v101
	v_cmp_gt_i32_e32 vcc, 0, v101
	s_nop 1
	v_cndmask_b32_e32 v96, v97, v96, vcc
	v_not_b32_e32 v97, v103
	v_cmp_gt_i32_e32 vcc, 0, v103
	s_nop 1
	v_cndmask_b32_e32 v97, v98, v97, vcc
	v_not_b32_e32 v98, v104
	v_cmp_gt_i32_e32 vcc, 0, v104
	s_nop 1
	v_cndmask_b32_e32 v136, v99, v98, vcc
	v_not_b32_e32 v98, v105
	v_or_b32_e32 v99, 0x80000000, v105
	v_cmp_gt_i32_e32 vcc, 0, v105
	s_nop 1
	v_cndmask_b32_e32 v137, v99, v98, vcc
	v_not_b32_e32 v98, v106
	v_or_b32_e32 v99, 0x80000000, v106
	v_cmp_gt_i32_e32 vcc, 0, v106
	s_nop 1
	v_cndmask_b32_e32 v138, v99, v98, vcc
	v_not_b32_e32 v98, v107
	v_or_b32_e32 v99, 0x80000000, v107
	v_cmp_gt_i32_e32 vcc, 0, v107
	s_nop 1
	v_cndmask_b32_e32 v139, v99, v98, vcc
	v_not_b32_e32 v98, v108
	v_or_b32_e32 v99, 0x80000000, v108
	v_cmp_gt_i32_e32 vcc, 0, v108
	s_nop 1
	v_cndmask_b32_e32 v140, v99, v98, vcc
	v_not_b32_e32 v98, v110
	v_or_b32_e32 v99, 0x80000000, v110
	v_cmp_gt_i32_e32 vcc, 0, v110
	s_nop 1
	v_cndmask_b32_e32 v141, v99, v98, vcc
	v_not_b32_e32 v98, v112
	v_or_b32_e32 v99, 0x80000000, v112
	v_cmp_gt_i32_e32 vcc, 0, v112
	s_nop 1
	v_cndmask_b32_e32 v142, v99, v98, vcc
	v_not_b32_e32 v98, v113
	v_or_b32_e32 v99, 0x80000000, v113
	v_cmp_gt_i32_e32 vcc, 0, v113
	s_nop 1
	v_cndmask_b32_e32 v143, v99, v98, vcc
	v_not_b32_e32 v98, v114
	v_or_b32_e32 v99, 0x80000000, v114
	v_cmp_gt_i32_e32 vcc, 0, v114
	s_nop 1
	v_cndmask_b32_e32 v144, v99, v98, vcc
	v_not_b32_e32 v98, v115
	v_or_b32_e32 v99, 0x80000000, v115
	v_cmp_gt_i32_e32 vcc, 0, v115
	s_nop 1
	v_cndmask_b32_e32 v145, v99, v98, vcc
	v_not_b32_e32 v98, v116
	v_or_b32_e32 v99, 0x80000000, v116
	v_cmp_gt_i32_e32 vcc, 0, v116
	s_nop 1
	v_cndmask_b32_e32 v146, v99, v98, vcc
	v_not_b32_e32 v98, v117
	v_or_b32_e32 v99, 0x80000000, v117
	v_cmp_gt_i32_e32 vcc, 0, v117
	s_nop 1
	v_cndmask_b32_e32 v147, v99, v98, vcc
	v_not_b32_e32 v98, v118
	v_or_b32_e32 v99, 0x80000000, v118
	v_cmp_gt_i32_e32 vcc, 0, v118
	s_nop 1
	v_cndmask_b32_e32 v132, v99, v98, vcc
	v_not_b32_e32 v98, v119
	v_or_b32_e32 v99, 0x80000000, v119
	v_cmp_gt_i32_e32 vcc, 0, v119
	s_nop 1
	v_cndmask_b32_e32 v148, v99, v98, vcc
	v_not_b32_e32 v98, v120
	v_or_b32_e32 v99, 0x80000000, v120
	v_cmp_gt_i32_e32 vcc, 0, v120
	s_nop 1
	v_cndmask_b32_e32 v149, v99, v98, vcc
	v_not_b32_e32 v98, v121
	v_or_b32_e32 v99, 0x80000000, v121
	v_cmp_gt_i32_e32 vcc, 0, v121
	s_nop 1
	v_cndmask_b32_e32 v150, v99, v98, vcc
	v_not_b32_e32 v98, v122
	v_or_b32_e32 v99, 0x80000000, v122
	v_cmp_gt_i32_e32 vcc, 0, v122
	s_nop 1
	v_cndmask_b32_e32 v151, v99, v98, vcc
	v_not_b32_e32 v98, v123
	v_or_b32_e32 v99, 0x80000000, v123
	v_cmp_gt_i32_e32 vcc, 0, v123
	s_nop 1
	v_cndmask_b32_e32 v123, v99, v98, vcc
	v_not_b32_e32 v98, v124
	v_or_b32_e32 v99, 0x80000000, v124
	v_cmp_gt_i32_e32 vcc, 0, v124
	s_nop 1
	v_cndmask_b32_e32 v152, v99, v98, vcc
	v_not_b32_e32 v98, v125
	v_or_b32_e32 v99, 0x80000000, v125
	v_cmp_gt_i32_e32 vcc, 0, v125
	s_nop 1
	v_cndmask_b32_e32 v153, v99, v98, vcc
	v_not_b32_e32 v98, v126
	v_or_b32_e32 v99, 0x80000000, v126
	v_cmp_gt_i32_e32 vcc, 0, v126
	s_nop 1
	v_cndmask_b32_e32 v154, v99, v98, vcc
	v_not_b32_e32 v98, v127
	v_or_b32_e32 v99, 0x80000000, v127
	v_cmp_gt_i32_e32 vcc, 0, v127
	s_nop 1
	v_cndmask_b32_e32 v155, v99, v98, vcc
	v_not_b32_e32 v98, v128
	v_or_b32_e32 v99, 0x80000000, v128
	v_cmp_gt_i32_e32 vcc, 0, v128
	s_nop 1
	v_cndmask_b32_e32 v156, v99, v98, vcc
	v_not_b32_e32 v98, v129
	v_or_b32_e32 v99, 0x80000000, v129
	v_cmp_gt_i32_e32 vcc, 0, v129
	s_nop 1
	v_cndmask_b32_e32 v157, v99, v98, vcc
	v_not_b32_e32 v98, v130
	v_or_b32_e32 v99, 0x80000000, v130
	v_cmp_gt_i32_e32 vcc, 0, v130
	v_cndmask_b32_e64 v130, v135, 0, s[80:81]
	v_readlane_b32 s80, v236, 49
	v_readlane_b32 s81, v236, 50
	v_cndmask_b32_e32 v158, v99, v98, vcc
	v_not_b32_e32 v98, v131
	v_cndmask_b32_e64 v129, 0, v70, s[80:81]
	v_readlane_b32 s80, v236, 53
	v_readlane_b32 s81, v236, 54
	v_or_b32_e32 v99, 0x80000000, v131
	v_cmp_gt_i32_e32 vcc, 0, v131
	v_cndmask_b32_e64 v128, 0, v71, s[80:81]
	v_readlane_b32 s80, v236, 55
	v_readlane_b32 s81, v236, 56
	v_cndmask_b32_e32 v131, v99, v98, vcc
	v_not_b32_e32 v98, v133
	v_cndmask_b32_e64 v127, 0, v72, s[80:81]
	v_readlane_b32 s80, v236, 57
	v_readlane_b32 s81, v236, 58
	v_or_b32_e32 v99, 0x80000000, v133
	v_cmp_gt_i32_e32 vcc, 0, v133
	v_cndmask_b32_e64 v126, 0, v73, s[80:81]
	v_readlane_b32 s80, v236, 59
	v_readlane_b32 s81, v236, 60
	v_cndmask_b32_e32 v133, v99, v98, vcc
	v_not_b32_e32 v98, v134
	v_cndmask_b32_e64 v125, 0, v74, s[80:81]
	v_readlane_b32 s80, v236, 61
	v_readlane_b32 s81, v236, 62
	v_or_b32_e32 v99, 0x80000000, v134
	v_cmp_gt_i32_e32 vcc, 0, v134
	v_cndmask_b32_e64 v124, 0, v75, s[80:81]
	v_readlane_b32 s80, v236, 63
	v_readlane_b32 s81, v235, 0
	v_cndmask_b32_e32 v134, v99, v98, vcc
	v_mov_b32_e32 v71, 0
	v_cndmask_b32_e64 v122, 0, v76, s[80:81]
	v_readlane_b32 s80, v235, 1
	v_readlane_b32 s81, v235, 2
	s_nop 1
	v_cndmask_b32_e64 v121, 0, v77, s[80:81]
	v_readlane_b32 s80, v235, 3
	v_readlane_b32 s81, v235, 4
	s_nop 1
	v_cndmask_b32_e64 v120, 0, v78, s[80:81]
	v_readlane_b32 s80, v235, 5
	v_readlane_b32 s81, v235, 6
	s_nop 1
	v_cndmask_b32_e64 v119, 0, v79, s[80:81]
	v_readlane_b32 s80, v235, 7
	v_readlane_b32 s81, v235, 8
	s_nop 1
	v_cndmask_b32_e64 v118, 0, v80, s[80:81]
	v_readlane_b32 s80, v235, 9
	v_readlane_b32 s81, v235, 10
	s_nop 1
	v_cndmask_b32_e64 v117, 0, v81, s[80:81]
	v_readlane_b32 s80, v235, 11
	v_readlane_b32 s81, v235, 12
	s_nop 1
	v_cndmask_b32_e64 v116, 0, v82, s[80:81]
	v_readlane_b32 s80, v235, 13
	v_readlane_b32 s81, v235, 14
	s_nop 1
	v_cndmask_b32_e64 v115, 0, v83, s[80:81]
	v_readlane_b32 s80, v235, 15
	v_readlane_b32 s81, v235, 16
	s_nop 1
	v_cndmask_b32_e64 v114, 0, v84, s[80:81]
	v_readlane_b32 s80, v235, 17
	v_readlane_b32 s81, v235, 18
	s_nop 1
	v_cndmask_b32_e64 v113, 0, v85, s[80:81]
	v_readlane_b32 s80, v235, 19
	v_readlane_b32 s81, v235, 20
	s_nop 1
	v_cndmask_b32_e64 v112, 0, v86, s[80:81]
	v_readlane_b32 s80, v235, 21
	v_readlane_b32 s81, v235, 22
	s_nop 1
	v_cndmask_b32_e64 v110, 0, v87, s[80:81]
	v_readlane_b32 s80, v235, 23
	v_readlane_b32 s81, v235, 24
	s_nop 1
	v_cndmask_b32_e64 v108, 0, v88, s[80:81]
	v_readlane_b32 s80, v235, 25
	v_readlane_b32 s81, v235, 26
	s_nop 1
	v_cndmask_b32_e64 v107, 0, v89, s[80:81]
	v_readlane_b32 s80, v235, 27
	v_readlane_b32 s81, v235, 28
	s_nop 1
	v_cndmask_b32_e64 v106, 0, v90, s[80:81]
	v_readlane_b32 s80, v235, 29
	v_readlane_b32 s81, v235, 30
	s_nop 1
	v_cndmask_b32_e64 v105, 0, v91, s[80:81]
	v_readlane_b32 s80, v235, 31
	v_readlane_b32 s81, v235, 32
	s_nop 1
	v_cndmask_b32_e64 v104, 0, v92, s[80:81]
	v_readlane_b32 s80, v235, 33
	v_readlane_b32 s81, v235, 34
	s_nop 1
	v_cndmask_b32_e64 v103, 0, v93, s[80:81]
	v_readlane_b32 s80, v235, 35
	v_readlane_b32 s81, v235, 36
	s_nop 1
	v_cndmask_b32_e64 v101, 0, v94, s[80:81]
	v_readlane_b32 s80, v235, 37
	v_readlane_b32 s81, v235, 38
	s_nop 1
	v_cndmask_b32_e64 v100, 0, v95, s[80:81]
	v_readlane_b32 s80, v235, 39
	v_readlane_b32 s81, v235, 40
	s_nop 1
	v_cndmask_b32_e64 v99, 0, v96, s[80:81]
	v_readlane_b32 s80, v235, 41
	v_readlane_b32 s81, v235, 42
	s_nop 1
	v_cndmask_b32_e64 v98, 0, v97, s[80:81]
	v_readlane_b32 s80, v235, 43
	v_readlane_b32 s81, v235, 44
	s_nop 1
	v_cndmask_b32_e64 v97, 0, v136, s[80:81]
	v_readlane_b32 s80, v235, 45
	v_readlane_b32 s81, v235, 46
	s_nop 1
	v_cndmask_b32_e64 v96, 0, v137, s[80:81]
	v_readlane_b32 s80, v235, 47
	v_readlane_b32 s81, v235, 48
	s_nop 1
	v_cndmask_b32_e64 v95, 0, v138, s[80:81]
	v_readlane_b32 s80, v235, 49
	v_readlane_b32 s81, v235, 50
	s_nop 1
	v_cndmask_b32_e64 v94, 0, v139, s[80:81]
	v_readlane_b32 s80, v235, 51
	v_readlane_b32 s81, v235, 52
	s_nop 1
	v_cndmask_b32_e64 v93, 0, v140, s[80:81]
	v_readlane_b32 s80, v235, 53
	v_readlane_b32 s81, v235, 54
	s_nop 1
	v_cndmask_b32_e64 v92, 0, v141, s[80:81]
	v_readlane_b32 s80, v235, 55
	v_readlane_b32 s81, v235, 56
	s_nop 1
	v_cndmask_b32_e64 v91, 0, v142, s[80:81]
	v_readlane_b32 s80, v235, 57
	v_readlane_b32 s81, v235, 58
	s_nop 1
	v_cndmask_b32_e64 v90, 0, v143, s[80:81]
	v_readlane_b32 s80, v235, 59
	v_readlane_b32 s81, v235, 60
	s_nop 1
	v_cndmask_b32_e64 v89, 0, v144, s[80:81]
	v_readlane_b32 s80, v235, 61
	v_readlane_b32 s81, v235, 62
	s_nop 1
	v_cndmask_b32_e64 v88, 0, v145, s[80:81]
	v_readlane_b32 s80, v235, 63
	v_readlane_b32 s81, v234, 0
	s_nop 1
	v_cndmask_b32_e64 v87, 0, v146, s[80:81]
	v_readlane_b32 s80, v234, 1
	v_readlane_b32 s81, v234, 2
	s_nop 1
	v_cndmask_b32_e64 v86, 0, v147, s[80:81]
	v_readlane_b32 s80, v234, 3
	v_readlane_b32 s81, v234, 4
	s_nop 1
	v_cndmask_b32_e64 v85, 0, v148, s[80:81]
	v_readlane_b32 s80, v234, 5
	v_readlane_b32 s81, v234, 6
	s_nop 1
	v_cndmask_b32_e64 v84, 0, v149, s[80:81]
	v_readlane_b32 s80, v234, 7
	v_readlane_b32 s81, v234, 8
	s_nop 1
	v_cndmask_b32_e64 v83, 0, v150, s[80:81]
	v_readlane_b32 s80, v234, 9
	v_readlane_b32 s81, v234, 10
	s_nop 1
	v_cndmask_b32_e64 v82, 0, v151, s[80:81]
	v_readlane_b32 s80, v234, 11
	v_readlane_b32 s81, v234, 12
	s_nop 1
	v_cndmask_b32_e64 v81, 0, v123, s[80:81]
	v_readlane_b32 s80, v234, 13
	v_readlane_b32 s81, v234, 14
	v_mov_b32_e32 v123, 31
	s_nop 0
	v_cndmask_b32_e64 v80, 0, v152, s[80:81]
	v_readlane_b32 s80, v234, 15
	v_readlane_b32 s81, v234, 16
	s_nop 1
	v_cndmask_b32_e64 v79, 0, v153, s[80:81]
	v_readlane_b32 s80, v234, 17
	v_readlane_b32 s81, v234, 18
	s_nop 1
	v_cndmask_b32_e64 v78, 0, v154, s[80:81]
	v_readlane_b32 s80, v234, 19
	v_readlane_b32 s81, v234, 20
	s_nop 1
	v_cndmask_b32_e64 v77, 0, v155, s[80:81]
	v_readlane_b32 s80, v234, 21
	v_readlane_b32 s81, v234, 22
	s_nop 1
	v_cndmask_b32_e64 v76, 0, v156, s[80:81]
	v_readlane_b32 s80, v234, 23
	v_readlane_b32 s81, v234, 24
	s_nop 1
	v_cndmask_b32_e64 v75, 0, v157, s[80:81]
	v_readlane_b32 s80, v234, 25
	v_readlane_b32 s81, v234, 26
	s_nop 1
	v_cndmask_b32_e64 v74, 0, v158, s[80:81]
	v_readlane_b32 s80, v234, 27
	v_readlane_b32 s81, v234, 28
	s_nop 1
	v_cndmask_b32_e64 v73, 0, v131, s[80:81]
	v_readlane_b32 s80, v234, 29
	v_readlane_b32 s81, v234, 30
	s_nop 1
	v_cndmask_b32_e64 v72, 0, v133, s[80:81]
	v_readlane_b32 s80, v234, 31
	v_readlane_b32 s81, v234, 32
	s_nop 1
	v_cndmask_b32_e64 v70, 0, v134, s[80:81]
	s_branch .LBB0_417
